# MoE combine loop: all 12 row loads of a token issued at the loop top (j=1..3 into spare regs), later per-j load/wait replaced by register copies
# speedup vs baseline: 1.0177x; 1.0058x over previous
; __device__ __forceinline__ void unpack8(u32x4 w, f32x4& v0, f32x4& v1) { v0 = (f32x4){bf_lo(w.x), bf_hi(w.x), bf_lo(w.y), bf_hi(w.y)}; v1 = (f32x4){bf_lo(w.z), bf_hi(w.z), bf_lo(w.w), bf_hi(w.w)}; }
; __global__ void __launch_bounds__(NWAVES * 64, 2) mk_fwd(Args a) {
;     ...
;             { for (int tok = gw; tok < NT; tok += ngw) { const int d0 = tokdest[tok * 2], d1 = tokdest[tok * 2 + 1]; float sq = 0.f;
; #pragma unroll
;                   for (int j = 0; j < 4; ++j) { const size_t o = (size_t)tok * DM + (lane + 64 * j) * 8; f32x4 x0, x1, p0, p1, q0, q1; epi::unpack8(*(const u32x4*)(XR + o), x0, x1);
;                       epi::unpack8(*(const u32x4*)(YB + (size_t)d0 * DM + (lane + 64 * j) * 8), p0, p1); epi::unpack8(*(const u32x4*)(YB + (size_t)d1 * DM + (lane + 64 * j) * 8), q0, q1);
;                       x0 += p0 + q0; x1 += p1 + q1;
.LBB0_2412:
	s_ashr_i32 s19, s18, 31
	s_lshl_b64 s[4:5], s[18:19], 2
	s_add_u32 s4, s8, s4
	s_addc_u32 s5, s9, s5
	global_load_dwordx2 v[34:35], v3, s[4:5]
	s_waitcnt lgkmcnt(0)
	v_lshl_add_u64 v[24:25], s[52:53], 0, v[22:23]
	v_add_co_u32_e32 v36, vcc, s40, v24
	s_nop 1
	v_addc_co_u32_e32 v37, vcc, 0, v25, vcc
	global_load_dwordx4 v[26:29], v[36:37], off
	s_waitcnt vmcnt(1)
	v_readfirstlane_b32 s36, v34
	s_ashr_i32 s37, s36, 31
	v_ashrrev_i32_e32 v41, 31, v35
	v_mov_b32_e32 v40, v35
	s_lshl_b64 s[4:5], s[36:37], 12
	v_lshlrev_b64 v[40:41], 12, v[40:41]
	v_lshl_add_u64 v[38:39], v[14:15], 0, s[4:5]
	v_lshl_add_u64 v[40:41], v[14:15], 0, v[40:41]
	global_load_dwordx4 v[30:33], v[38:39], off
	global_load_dwordx4 v[42:45], v[40:41], off
	global_load_dwordx4 v[132:135], v[36:37], off offset:1024
	global_load_dwordx4 v[136:139], v[38:39], off offset:1024
	global_load_dwordx4 v[140:143], v[40:41], off offset:1024
	global_load_dwordx4 v[144:147], v[36:37], off offset:2048
	global_load_dwordx4 v[148:151], v[38:39], off offset:2048
	global_load_dwordx4 v[152:155], v[40:41], off offset:2048
	global_load_dwordx4 v[156:159], v[36:37], off offset:3072
	global_load_dwordx4 v[160:163], v[38:39], off offset:3072
	global_load_dwordx4 v[164:167], v[40:41], off offset:3072
	s_waitcnt vmcnt(2)
	v_lshlrev_b32_e32 v46, 16, v28
	v_and_b32_e32 v47, 0xffff0000, v28
	v_lshlrev_b32_e32 v48, 16, v29
	v_and_b32_e32 v49, 0xffff0000, v29
	v_readfirstlane_b32 s19, v35
	v_lshlrev_b32_e32 v34, 16, v26
	v_and_b32_e32 v35, 0xffff0000, v26
	v_lshlrev_b32_e32 v26, 16, v27
	v_and_b32_e32 v27, 0xffff0000, v27
	s_cmpk_gt_i32 s36, 0x3fff
	s_cselect_b64 s[6:7], -1, 0
	s_cmpk_lt_i32 s36, 0x4000
	s_waitcnt vmcnt(1)
	v_lshlrev_b32_e32 v28, 16, v30
	v_and_b32_e32 v29, 0xffff0000, v30
	v_lshlrev_b32_e32 v30, 16, v31
	v_and_b32_e32 v31, 0xffff0000, v31
	v_lshlrev_b32_e32 v50, 16, v32
	v_and_b32_e32 v51, 0xffff0000, v32
	v_lshlrev_b32_e32 v32, 16, v33
	v_and_b32_e32 v33, 0xffff0000, v33
	s_waitcnt vmcnt(0)
	v_lshlrev_b32_e32 v52, 16, v42
	v_and_b32_e32 v53, 0xffff0000, v42
	v_lshlrev_b32_e32 v42, 16, v43
	v_and_b32_e32 v43, 0xffff0000, v43
	v_lshlrev_b32_e32 v54, 16, v44
	v_and_b32_e32 v55, 0xffff0000, v44
	v_lshlrev_b32_e32 v44, 16, v45
	v_and_b32_e32 v45, 0xffff0000, v45
	v_pk_add_f32 v[28:29], v[28:29], v[52:53]
	v_pk_add_f32 v[30:31], v[30:31], v[42:43]
	v_pk_add_f32 v[42:43], v[50:51], v[54:55]
	v_pk_add_f32 v[32:33], v[32:33], v[44:45]
	v_pk_add_f32 v[26:27], v[30:31], v[26:27]
	v_pk_add_f32 v[28:29], v[28:29], v[34:35]
	v_pk_add_f32 v[30:31], v[32:33], v[48:49]
	v_pk_add_f32 v[32:33], v[42:43], v[46:47]
	s_cbranch_scc1 .LBB0_2414
	s_add_i32 s12, s36, 0xffffc000
	s_lshl_b64 s[4:5], s[12:13], 12
	v_lshl_add_u64 v[34:35], v[4:5], 0, s[4:5]
	v_add_co_u32_e32 v46, vcc, s41, v34
	global_load_dwordx4 v[42:45], v[34:35], off
	s_nop 0
	v_addc_co_u32_e32 v47, vcc, 0, v35, vcc
	global_load_dwordx4 v[46:49], v[46:47], off
	v_add_co_u32_e32 v34, vcc, s44, v34
	s_waitcnt vmcnt(1)
	v_lshlrev_b32_e32 v54, 16, v44
	v_addc_co_u32_e32 v35, vcc, 0, v35, vcc
	global_load_dwordx4 v[50:53], v[34:35], off
	v_lshlrev_b32_e32 v34, 16, v42
	v_and_b32_e32 v35, 0xffff0000, v42
	v_lshlrev_b32_e32 v42, 16, v43
	v_and_b32_e32 v43, 0xffff0000, v43
	v_and_b32_e32 v55, 0xffff0000, v44
	v_lshlrev_b32_e32 v44, 16, v45
	v_and_b32_e32 v45, 0xffff0000, v45
	v_pk_add_f32 v[26:27], v[26:27], v[42:43]
	v_pk_add_f32 v[28:29], v[28:29], v[34:35]
	v_pk_add_f32 v[30:31], v[30:31], v[44:45]
	v_pk_add_f32 v[32:33], v[32:33], v[54:55]
	s_waitcnt vmcnt(1)
	v_lshlrev_b32_e32 v34, 16, v46
	v_and_b32_e32 v35, 0xffff0000, v46
	v_lshlrev_b32_e32 v42, 16, v47
	v_and_b32_e32 v43, 0xffff0000, v47
	v_lshlrev_b32_e32 v44, 16, v48
	v_and_b32_e32 v45, 0xffff0000, v48
	v_lshlrev_b32_e32 v46, 16, v49
	v_and_b32_e32 v47, 0xffff0000, v49
	v_pk_add_f32 v[28:29], v[28:29], v[34:35]
	v_pk_add_f32 v[26:27], v[26:27], v[42:43]
	v_pk_add_f32 v[32:33], v[32:33], v[44:45]
	v_pk_add_f32 v[30:31], v[30:31], v[46:47]
	s_waitcnt vmcnt(0)
	v_lshlrev_b32_e32 v48, 16, v50
	v_and_b32_e32 v49, 0xffff0000, v50
	v_lshlrev_b32_e32 v50, 16, v51
	v_and_b32_e32 v51, 0xffff0000, v51
	v_lshlrev_b32_e32 v54, 16, v52
	v_and_b32_e32 v55, 0xffff0000, v52
	v_lshlrev_b32_e32 v52, 16, v53
	v_and_b32_e32 v53, 0xffff0000, v53
	v_pk_add_f32 v[26:27], v[26:27], v[50:51]
	v_pk_add_f32 v[28:29], v[28:29], v[48:49]
	v_pk_add_f32 v[30:31], v[30:31], v[52:53]
	v_pk_add_f32 v[32:33], v[32:33], v[54:55]

; __device__ __forceinline__ u32x4 pack8(f32x4 v0, f32x4 v1) { u32x4 w; w.x = cvt_pk_bf16(v0[0], v0[1]); w.y = cvt_pk_bf16(v0[2], v0[3]); w.z = cvt_pk_bf16(v1[0], v1[1]); w.w = cvt_pk_bf16(v1[2], v1[3]); return w; }
; __device__ __forceinline__ void unpack8(u32x4 w, f32x4& v0, f32x4& v1) { v0 = (f32x4){bf_lo(w.x), bf_hi(w.x), bf_lo(w.y), bf_hi(w.y)}; v1 = (f32x4){bf_lo(w.z), bf_hi(w.z), bf_lo(w.w), bf_hi(w.w)}; }
; __global__ void __launch_bounds__(NWAVES * 64, 2) mk_fwd(Args a) {
;     ...
;                   for (int j = 0; j < 4; ++j) { const size_t o = (size_t)tok * DM + (lane + 64 * j) * 8; f32x4 x0, x1, p0, p1, q0, q1; epi::unpack8(*(const u32x4*)(XR + o), x0, x1);
;                       epi::unpack8(*(const u32x4*)(YB + (size_t)d0 * DM + (lane + 64 * j) * 8), p0, p1); epi::unpack8(*(const u32x4*)(YB + (size_t)d1 * DM + (lane + 64 * j) * 8), q0, q1);
;                       x0 += p0 + q0; x1 += p1 + q1;
; #pragma unroll
;                       for (int dd = 0; dd < 2; ++dd) { const int d = dd ? d1 : d0; if (d >= 16384) {
; #pragma unroll
;                           for (int s = 0; s < 3; ++s) { epi::unpack8(*(const u32x4*)((const bf16_t*)(ws + wsm::YBX) + ((size_t)s * 2048 + (d - 16384)) * DM + (lane + 64 * j) * 8), p0, p1); x0 += p0; x1 += p1; } } } *(u32x4*)(XR + o) = epi::pack8(x0, x1);
;                       const float* gp = a.in[28] + DM + (lane + 64 * j) * 8; const f32x4 y0 = x0 * *(const f32x4*)gp, y1 = x1 * *(const f32x4*)(gp + 4);
.LBB0_2416:
	v_lshl_add_u64 v[34:35], v[24:25], 0, s[20:21]
	v_cvt_pk_bf16_f32 v42, v28, v29
	v_cvt_pk_bf16_f32 v43, v26, v27
	v_cvt_pk_bf16_f32 v44, v32, v33
	v_cvt_pk_bf16_f32 v45, v30, v31
	global_store_dwordx4 v[34:35], v[42:45], off
	s_nop 1
	v_mov_b32_e32 v42, v100
	v_mov_b32_e32 v43, v101
	v_mov_b32_e32 v44, v102
	v_mov_b32_e32 v45, v103
	s_nop 0
	s_nop 1
	v_mov_b32_e32 v46, v104
	v_mov_b32_e32 v47, v105
	v_mov_b32_e32 v48, v106
	v_mov_b32_e32 v49, v107
	v_cndmask_b32_e64 v2, 0, 1, s[6:7]
	v_cmp_ne_u32_e64 s[4:5], 1, v2
	s_nop 0
	v_pk_mul_f32 v[34:35], v[26:27], v[44:45]
	v_pk_mul_f32 v[42:43], v[28:29], v[42:43]
	s_nop 0
	v_pk_mul_f32 v[44:45], v[32:33], v[46:47]
	v_cvt_pk_bf16_f32 v42, v42, v43
	v_cvt_pk_bf16_f32 v43, v34, v35
	v_add_co_u32_e32 v34, vcc, s45, v24
	v_pk_mul_f32 v[48:49], v[30:31], v[48:49]
	s_nop 0
	v_addc_co_u32_e32 v35, vcc, 0, v25, vcc
	v_cvt_pk_bf16_f32 v44, v44, v45
	v_cvt_pk_bf16_f32 v45, v48, v49
	global_store_dwordx4 v[34:35], v[42:45], off
	s_nop 1
	v_mov_b32_e32 v46, v132
	v_mov_b32_e32 v47, v133
	v_mov_b32_e32 v48, v134
	v_mov_b32_e32 v49, v135
	s_nop 0
	s_nop 1
	v_mov_b32_e32 v42, v136
	v_mov_b32_e32 v43, v137
	v_mov_b32_e32 v44, v138
	v_mov_b32_e32 v45, v139
	s_nop 1
	v_mov_b32_e32 v50, v140
	v_mov_b32_e32 v51, v141
	v_mov_b32_e32 v52, v142
	v_mov_b32_e32 v53, v143
	s_andn2_b64 vcc, exec, s[6:7]
	s_nop 0
	v_lshlrev_b32_e32 v54, 16, v46
	s_nop 0
	v_lshlrev_b32_e32 v58, 16, v42
	v_and_b32_e32 v59, 0xffff0000, v42
	v_lshlrev_b32_e32 v42, 16, v43
	v_and_b32_e32 v43, 0xffff0000, v43
	v_lshlrev_b32_e32 v60, 16, v44
	v_and_b32_e32 v61, 0xffff0000, v44
	v_lshlrev_b32_e32 v44, 16, v45
	v_and_b32_e32 v45, 0xffff0000, v45
	s_nop 0
	v_lshlrev_b32_e32 v62, 16, v50
	v_and_b32_e32 v63, 0xffff0000, v50
	v_lshlrev_b32_e32 v50, 16, v51
	v_and_b32_e32 v51, 0xffff0000, v51
	v_lshlrev_b32_e32 v64, 16, v52
	v_and_b32_e32 v65, 0xffff0000, v52
	v_lshlrev_b32_e32 v52, 16, v53
	v_and_b32_e32 v53, 0xffff0000, v53
	v_and_b32_e32 v55, 0xffff0000, v46
	v_lshlrev_b32_e32 v46, 16, v47
	v_and_b32_e32 v47, 0xffff0000, v47
	v_lshlrev_b32_e32 v56, 16, v48
	v_and_b32_e32 v57, 0xffff0000, v48
	v_lshlrev_b32_e32 v48, 16, v49
	v_and_b32_e32 v49, 0xffff0000, v49
	v_pk_add_f32 v[58:59], v[58:59], v[62:63]
	v_pk_add_f32 v[42:43], v[42:43], v[50:51]
	v_pk_add_f32 v[50:51], v[60:61], v[64:65]
	v_pk_add_f32 v[52:53], v[44:45], v[52:53]
	v_pk_add_f32 v[42:43], v[42:43], v[46:47]
	v_pk_add_f32 v[44:45], v[58:59], v[54:55]
	v_pk_add_f32 v[46:47], v[52:53], v[48:49]
	v_pk_add_f32 v[48:49], v[50:51], v[56:57]
	s_cbranch_vccnz .LBB0_2418
	s_add_i32 s12, s36, 0xffffc000
	s_lshl_b64 s[6:7], s[12:13], 12
	v_lshl_add_u64 v[58:59], v[16:17], 0, s[6:7]
	v_add_co_u32_e32 v54, vcc, s41, v58
	global_load_dwordx4 v[50:53], v[58:59], off
	s_nop 0
	v_addc_co_u32_e32 v55, vcc, 0, v59, vcc
	global_load_dwordx4 v[54:57], v[54:55], off
	v_add_co_u32_e32 v58, vcc, s44, v58
	s_waitcnt vmcnt(1)
	v_lshlrev_b32_e32 v62, 16, v50
	v_addc_co_u32_e32 v59, vcc, 0, v59, vcc
	global_load_dwordx4 v[58:61], v[58:59], off
	v_and_b32_e32 v63, 0xffff0000, v50
	v_lshlrev_b32_e32 v50, 16, v51
	v_and_b32_e32 v51, 0xffff0000, v51
	v_lshlrev_b32_e32 v64, 16, v52
	v_and_b32_e32 v65, 0xffff0000, v52
	v_lshlrev_b32_e32 v52, 16, v53
	v_and_b32_e32 v53, 0xffff0000, v53
	v_pk_add_f32 v[42:43], v[42:43], v[50:51]
	v_pk_add_f32 v[44:45], v[44:45], v[62:63]
	v_pk_add_f32 v[46:47], v[46:47], v[52:53]
	v_pk_add_f32 v[48:49], v[48:49], v[64:65]
	s_waitcnt vmcnt(1)
	v_lshlrev_b32_e32 v50, 16, v54
	v_and_b32_e32 v51, 0xffff0000, v54
	v_lshlrev_b32_e32 v52, 16, v55
	v_and_b32_e32 v53, 0xffff0000, v55
	v_lshlrev_b32_e32 v54, 16, v56
	v_and_b32_e32 v55, 0xffff0000, v56
	v_lshlrev_b32_e32 v56, 16, v57
	v_and_b32_e32 v57, 0xffff0000, v57
	v_pk_add_f32 v[44:45], v[44:45], v[50:51]
	v_pk_add_f32 v[42:43], v[42:43], v[52:53]
	v_pk_add_f32 v[48:49], v[48:49], v[54:55]
	v_pk_add_f32 v[46:47], v[46:47], v[56:57]
	s_waitcnt vmcnt(0)
	v_lshlrev_b32_e32 v62, 16, v58
	v_and_b32_e32 v63, 0xffff0000, v58
	v_lshlrev_b32_e32 v58, 16, v59
	v_and_b32_e32 v59, 0xffff0000, v59
	v_lshlrev_b32_e32 v64, 16, v60
	v_and_b32_e32 v65, 0xffff0000, v60
	v_lshlrev_b32_e32 v60, 16, v61
	v_and_b32_e32 v61, 0xffff0000, v61
	v_pk_add_f32 v[42:43], v[42:43], v[58:59]
	v_pk_add_f32 v[44:45], v[44:45], v[62:63]
	v_pk_add_f32 v[46:47], v[46:47], v[60:61]
	v_pk_add_f32 v[48:49], v[48:49], v[64:65]

; __device__ __forceinline__ unsigned pk4_fp8(float a, float b, float c, float d) { int w = 0; w = __builtin_amdgcn_cvt_pk_fp8_f32(a, b, w, false); w = __builtin_amdgcn_cvt_pk_fp8_f32(c, d, w, true); return (unsigned)w; }
; __device__ __forceinline__ u32x4 pack8(f32x4 v0, f32x4 v1) { u32x4 w; w.x = cvt_pk_bf16(v0[0], v0[1]); w.y = cvt_pk_bf16(v0[2], v0[3]); w.z = cvt_pk_bf16(v1[0], v1[1]); w.w = cvt_pk_bf16(v1[2], v1[3]); return w; }
; __device__ __forceinline__ void unpack8(u32x4 w, f32x4& v0, f32x4& v1) { v0 = (f32x4){bf_lo(w.x), bf_hi(w.x), bf_lo(w.y), bf_hi(w.y)}; v1 = (f32x4){bf_lo(w.z), bf_hi(w.z), bf_lo(w.w), bf_hi(w.w)}; }
; __global__ void __launch_bounds__(NWAVES * 64, 2) mk_fwd(Args a) {
;     ...
;                   for (int j = 0; j < 4; ++j) { const size_t o = (size_t)tok * DM + (lane + 64 * j) * 8; f32x4 x0, x1, p0, p1, q0, q1; epi::unpack8(*(const u32x4*)(XR + o), x0, x1);
;                       epi::unpack8(*(const u32x4*)(YB + (size_t)d0 * DM + (lane + 64 * j) * 8), p0, p1); epi::unpack8(*(const u32x4*)(YB + (size_t)d1 * DM + (lane + 64 * j) * 8), q0, q1);
;                       x0 += p0 + q0; x1 += p1 + q1;
; #pragma unroll
;                       for (int dd = 0; dd < 2; ++dd) { const int d = dd ? d1 : d0; if (d >= 16384) {
; #pragma unroll
;                           for (int s = 0; s < 3; ++s) { epi::unpack8(*(const u32x4*)((const bf16_t*)(ws + wsm::YBX) + ((size_t)s * 2048 + (d - 16384)) * DM + (lane + 64 * j) * 8), p0, p1); x0 += p0; x1 += p1; } } } *(u32x4*)(XR + o) = epi::pack8(x0, x1);
;                       const float* gp = a.in[28] + DM + (lane + 64 * j) * 8; const f32x4 y0 = x0 * *(const f32x4*)gp, y1 = x1 * *(const f32x4*)(gp + 4);
;                       if constexpr (F8P) *(u32x2*)((unsigned char*)x2b + o) = (u32x2){pk4_fp8(y0[0], y0[1], y0[2], y0[3]), pk4_fp8(y1[0], y1[1], y1[2], y1[3])}; else *(u32x4*)(x2b + o) = epi::pack8(y0, y1);
.LBB0_2420:
	v_lshl_add_u64 v[54:55], v[24:25], 0, s[22:23]
	v_cvt_pk_bf16_f32 v50, v44, v45
	v_cvt_pk_bf16_f32 v51, v42, v43
	v_cvt_pk_bf16_f32 v52, v48, v49
	v_cvt_pk_bf16_f32 v53, v46, v47
	global_store_dwordx4 v[54:55], v[50:53], off
	s_nop 1
	v_mov_b32_e32 v50, v108
	v_mov_b32_e32 v51, v109
	v_mov_b32_e32 v52, v110
	v_mov_b32_e32 v53, v111
	s_nop 0
	s_nop 1
	v_mov_b32_e32 v54, v112
	v_mov_b32_e32 v55, v113
	v_mov_b32_e32 v56, v114
	v_mov_b32_e32 v57, v115
	s_and_b64 vcc, exec, s[4:5]
	s_nop 0
	v_pk_mul_f32 v[52:53], v[42:43], v[52:53]
	v_pk_mul_f32 v[50:51], v[44:45], v[50:51]
	s_nop 0
	v_pk_mul_f32 v[56:57], v[46:47], v[56:57]
	v_pk_mul_f32 v[54:55], v[48:49], v[54:55]
	v_cvt_pk_bf16_f32 v50, v50, v51
	v_cvt_pk_bf16_f32 v51, v52, v53
	s_nop 0
	v_cvt_pk_bf16_f32 v52, v54, v55
	v_cvt_pk_bf16_f32 v53, v56, v57
	global_store_dwordx4 v[34:35], v[50:53], off offset:1024
	s_nop 1
	v_mov_b32_e32 v54, v144
	v_mov_b32_e32 v55, v145
	v_mov_b32_e32 v56, v146
	v_mov_b32_e32 v57, v147
	s_nop 0
	s_nop 1
	v_mov_b32_e32 v50, v148
	v_mov_b32_e32 v51, v149
	v_mov_b32_e32 v52, v150
	v_mov_b32_e32 v53, v151
	s_nop 1
	v_mov_b32_e32 v58, v152
	v_mov_b32_e32 v59, v153
	v_mov_b32_e32 v60, v154
	v_mov_b32_e32 v61, v155
	s_nop 0
	v_lshlrev_b32_e32 v66, 16, v50
	v_and_b32_e32 v67, 0xffff0000, v50
	v_lshlrev_b32_e32 v50, 16, v51
	v_and_b32_e32 v51, 0xffff0000, v51
	v_lshlrev_b32_e32 v68, 16, v52
	v_and_b32_e32 v69, 0xffff0000, v52
	v_lshlrev_b32_e32 v52, 16, v53
	v_and_b32_e32 v53, 0xffff0000, v53
	s_nop 0
	v_lshlrev_b32_e32 v70, 16, v58
	v_and_b32_e32 v71, 0xffff0000, v58
	v_lshlrev_b32_e32 v58, 16, v59
	v_and_b32_e32 v59, 0xffff0000, v59
	v_lshlrev_b32_e32 v72, 16, v60
	v_and_b32_e32 v73, 0xffff0000, v60
	v_lshlrev_b32_e32 v60, 16, v61
	v_and_b32_e32 v61, 0xffff0000, v61
	v_lshlrev_b32_e32 v62, 16, v54
	v_and_b32_e32 v63, 0xffff0000, v54
	v_lshlrev_b32_e32 v54, 16, v55
	v_and_b32_e32 v55, 0xffff0000, v55
	v_lshlrev_b32_e32 v64, 16, v56
	v_and_b32_e32 v65, 0xffff0000, v56
	v_lshlrev_b32_e32 v56, 16, v57
	v_and_b32_e32 v57, 0xffff0000, v57
	v_pk_add_f32 v[66:67], v[66:67], v[70:71]
	v_pk_add_f32 v[50:51], v[50:51], v[58:59]
	v_pk_add_f32 v[58:59], v[68:69], v[72:73]
	v_pk_add_f32 v[60:61], v[52:53], v[60:61]
	v_pk_add_f32 v[50:51], v[50:51], v[54:55]
	v_pk_add_f32 v[52:53], v[66:67], v[62:63]
	v_pk_add_f32 v[54:55], v[60:61], v[56:57]
	v_pk_add_f32 v[56:57], v[58:59], v[64:65]
	s_cbranch_vccnz .LBB0_2422
	s_add_i32 s12, s36, 0xffffc000
	s_lshl_b64 s[38:39], s[12:13], 12
	v_lshl_add_u64 v[66:67], v[18:19], 0, s[38:39]
	v_add_co_u32_e32 v62, vcc, s41, v66
	global_load_dwordx4 v[58:61], v[66:67], off
	s_nop 0
	v_addc_co_u32_e32 v63, vcc, 0, v67, vcc
	global_load_dwordx4 v[62:65], v[62:63], off
	v_add_co_u32_e32 v66, vcc, s44, v66
	s_waitcnt vmcnt(1)
	v_lshlrev_b32_e32 v70, 16, v58
	v_addc_co_u32_e32 v67, vcc, 0, v67, vcc
	global_load_dwordx4 v[66:69], v[66:67], off
	v_and_b32_e32 v71, 0xffff0000, v58
	v_lshlrev_b32_e32 v58, 16, v59
	v_and_b32_e32 v59, 0xffff0000, v59
	v_lshlrev_b32_e32 v72, 16, v60
	v_and_b32_e32 v73, 0xffff0000, v60
	v_lshlrev_b32_e32 v60, 16, v61
	v_and_b32_e32 v61, 0xffff0000, v61
	v_pk_add_f32 v[50:51], v[50:51], v[58:59]
	v_pk_add_f32 v[52:53], v[52:53], v[70:71]
	v_pk_add_f32 v[54:55], v[54:55], v[60:61]
	v_pk_add_f32 v[56:57], v[56:57], v[72:73]
	s_waitcnt vmcnt(1)
	v_lshlrev_b32_e32 v58, 16, v62
	v_and_b32_e32 v59, 0xffff0000, v62
	v_lshlrev_b32_e32 v60, 16, v63
	v_and_b32_e32 v61, 0xffff0000, v63
	v_lshlrev_b32_e32 v62, 16, v64
	v_and_b32_e32 v63, 0xffff0000, v64
	v_lshlrev_b32_e32 v64, 16, v65
	v_and_b32_e32 v65, 0xffff0000, v65
	v_pk_add_f32 v[52:53], v[52:53], v[58:59]
	v_pk_add_f32 v[50:51], v[50:51], v[60:61]
	v_pk_add_f32 v[56:57], v[56:57], v[62:63]
	v_pk_add_f32 v[54:55], v[54:55], v[64:65]
	s_waitcnt vmcnt(0)
	v_lshlrev_b32_e32 v70, 16, v66
	v_and_b32_e32 v71, 0xffff0000, v66
	v_lshlrev_b32_e32 v66, 16, v67
	v_and_b32_e32 v67, 0xffff0000, v67
	v_lshlrev_b32_e32 v72, 16, v68
	v_and_b32_e32 v73, 0xffff0000, v68
	v_lshlrev_b32_e32 v68, 16, v69
	v_and_b32_e32 v69, 0xffff0000, v69
	v_pk_add_f32 v[50:51], v[50:51], v[66:67]
	v_pk_add_f32 v[52:53], v[52:53], v[70:71]
	v_pk_add_f32 v[54:55], v[54:55], v[68:69]
	v_pk_add_f32 v[56:57], v[56:57], v[72:73]

; __device__ __forceinline__ unsigned pk4_fp8(float a, float b, float c, float d) { int w = 0; w = __builtin_amdgcn_cvt_pk_fp8_f32(a, b, w, false); w = __builtin_amdgcn_cvt_pk_fp8_f32(c, d, w, true); return (unsigned)w; }
; __device__ __forceinline__ u32x4 pack8(f32x4 v0, f32x4 v1) { u32x4 w; w.x = cvt_pk_bf16(v0[0], v0[1]); w.y = cvt_pk_bf16(v0[2], v0[3]); w.z = cvt_pk_bf16(v1[0], v1[1]); w.w = cvt_pk_bf16(v1[2], v1[3]); return w; }
; __device__ __forceinline__ void unpack8(u32x4 w, f32x4& v0, f32x4& v1) { v0 = (f32x4){bf_lo(w.x), bf_hi(w.x), bf_lo(w.y), bf_hi(w.y)}; v1 = (f32x4){bf_lo(w.z), bf_hi(w.z), bf_lo(w.w), bf_hi(w.w)}; }
; __global__ void __launch_bounds__(NWAVES * 64, 2) mk_fwd(Args a) {
;     ...
;                   for (int j = 0; j < 4; ++j) { const size_t o = (size_t)tok * DM + (lane + 64 * j) * 8; f32x4 x0, x1, p0, p1, q0, q1; epi::unpack8(*(const u32x4*)(XR + o), x0, x1);
;                       epi::unpack8(*(const u32x4*)(YB + (size_t)d0 * DM + (lane + 64 * j) * 8), p0, p1); epi::unpack8(*(const u32x4*)(YB + (size_t)d1 * DM + (lane + 64 * j) * 8), q0, q1);
;                       x0 += p0 + q0; x1 += p1 + q1;
; #pragma unroll
;                       for (int dd = 0; dd < 2; ++dd) { const int d = dd ? d1 : d0; if (d >= 16384) {
; #pragma unroll
;                           for (int s = 0; s < 3; ++s) { epi::unpack8(*(const u32x4*)((const bf16_t*)(ws + wsm::YBX) + ((size_t)s * 2048 + (d - 16384)) * DM + (lane + 64 * j) * 8), p0, p1); x0 += p0; x1 += p1; } } } *(u32x4*)(XR + o) = epi::pack8(x0, x1);
;                       const float* gp = a.in[28] + DM + (lane + 64 * j) * 8; const f32x4 y0 = x0 * *(const f32x4*)gp, y1 = x1 * *(const f32x4*)(gp + 4);
;                       if constexpr (F8P) *(u32x2*)((unsigned char*)x2b + o) = (u32x2){pk4_fp8(y0[0], y0[1], y0[2], y0[3]), pk4_fp8(y1[0], y1[1], y1[2], y1[3])}; else *(u32x4*)(x2b + o) = epi::pack8(y0, y1);
.LBB0_2424:
	v_lshl_add_u64 v[62:63], v[24:25], 0, s[24:25]
	v_cvt_pk_bf16_f32 v58, v52, v53
	v_cvt_pk_bf16_f32 v59, v50, v51
	v_cvt_pk_bf16_f32 v60, v56, v57
	v_cvt_pk_bf16_f32 v61, v54, v55
	global_store_dwordx4 v[62:63], v[58:61], off
	s_nop 1
	v_mov_b32_e32 v58, v116
	v_mov_b32_e32 v59, v117
	v_mov_b32_e32 v60, v118
	v_mov_b32_e32 v61, v119
	s_nop 0
	s_nop 1
	v_mov_b32_e32 v62, v120
	v_mov_b32_e32 v63, v121
	v_mov_b32_e32 v64, v122
	v_mov_b32_e32 v65, v123
	s_and_b64 vcc, exec, s[4:5]
	s_nop 0
	v_pk_mul_f32 v[60:61], v[50:51], v[60:61]
	v_pk_mul_f32 v[58:59], v[52:53], v[58:59]
	s_nop 0
	v_pk_mul_f32 v[64:65], v[54:55], v[64:65]
	v_pk_mul_f32 v[62:63], v[56:57], v[62:63]
	v_cvt_pk_bf16_f32 v58, v58, v59
	v_cvt_pk_bf16_f32 v59, v60, v61
	s_nop 0
	v_cvt_pk_bf16_f32 v60, v62, v63
	v_cvt_pk_bf16_f32 v61, v64, v65
	global_store_dwordx4 v[34:35], v[58:61], off offset:2048
	s_nop 1
	v_mov_b32_e32 v62, v156
	v_mov_b32_e32 v63, v157
	v_mov_b32_e32 v64, v158
	v_mov_b32_e32 v65, v159
	s_nop 0
	s_nop 1
	v_mov_b32_e32 v36, v160
	v_mov_b32_e32 v37, v161
	v_mov_b32_e32 v38, v162
	v_mov_b32_e32 v39, v163
	s_nop 0
	s_nop 1
	v_mov_b32_e32 v58, v164
	v_mov_b32_e32 v59, v165
	v_mov_b32_e32 v60, v166
	v_mov_b32_e32 v61, v167
	s_nop 0
	v_lshlrev_b32_e32 v68, 16, v36
	v_and_b32_e32 v69, 0xffff0000, v36
	v_lshlrev_b32_e32 v36, 16, v37
	v_and_b32_e32 v37, 0xffff0000, v37
	v_lshlrev_b32_e32 v70, 16, v38
	v_and_b32_e32 v71, 0xffff0000, v38
	v_lshlrev_b32_e32 v38, 16, v39
	v_and_b32_e32 v39, 0xffff0000, v39
	s_nop 0
	v_lshlrev_b32_e32 v72, 16, v58
	v_and_b32_e32 v73, 0xffff0000, v58
	v_lshlrev_b32_e32 v58, 16, v59
	v_and_b32_e32 v59, 0xffff0000, v59
	v_lshlrev_b32_e32 v74, 16, v60
	v_and_b32_e32 v75, 0xffff0000, v60
	v_lshlrev_b32_e32 v60, 16, v61
	v_and_b32_e32 v61, 0xffff0000, v61
	v_lshlrev_b32_e32 v40, 16, v62
	v_and_b32_e32 v41, 0xffff0000, v62
	v_lshlrev_b32_e32 v62, 16, v63
	v_and_b32_e32 v63, 0xffff0000, v63
	v_lshlrev_b32_e32 v66, 16, v64
	v_and_b32_e32 v67, 0xffff0000, v64
	v_lshlrev_b32_e32 v64, 16, v65
	v_and_b32_e32 v65, 0xffff0000, v65
	v_pk_add_f32 v[68:69], v[68:69], v[72:73]
	v_pk_add_f32 v[36:37], v[36:37], v[58:59]
	v_pk_add_f32 v[58:59], v[70:71], v[74:75]
	v_pk_add_f32 v[60:61], v[38:39], v[60:61]
	v_pk_add_f32 v[38:39], v[36:37], v[62:63]
	v_pk_add_f32 v[36:37], v[68:69], v[40:41]
	v_pk_add_f32 v[40:41], v[60:61], v[64:65]
	v_pk_add_f32 v[58:59], v[58:59], v[66:67]
	s_cbranch_vccnz .LBB0_2426
	s_add_i32 s12, s36, 0xffffc000
	s_lshl_b64 s[4:5], s[12:13], 12
	v_lshl_add_u64 v[68:69], v[20:21], 0, s[4:5]
	v_add_co_u32_e32 v64, vcc, s41, v68
	global_load_dwordx4 v[60:63], v[68:69], off
	s_nop 0
	v_addc_co_u32_e32 v65, vcc, 0, v69, vcc
	global_load_dwordx4 v[64:67], v[64:65], off
	v_add_co_u32_e32 v68, vcc, s44, v68
	s_waitcnt vmcnt(1)
	v_lshlrev_b32_e32 v72, 16, v60
	v_addc_co_u32_e32 v69, vcc, 0, v69, vcc
	global_load_dwordx4 v[68:71], v[68:69], off
	v_and_b32_e32 v73, 0xffff0000, v60
	v_lshlrev_b32_e32 v60, 16, v61
	v_and_b32_e32 v61, 0xffff0000, v61
	v_lshlrev_b32_e32 v74, 16, v62
	v_and_b32_e32 v75, 0xffff0000, v62
	v_lshlrev_b32_e32 v62, 16, v63
	v_and_b32_e32 v63, 0xffff0000, v63
	v_pk_add_f32 v[38:39], v[38:39], v[60:61]
	v_pk_add_f32 v[36:37], v[36:37], v[72:73]
	v_pk_add_f32 v[40:41], v[40:41], v[62:63]
	v_pk_add_f32 v[58:59], v[58:59], v[74:75]
	s_waitcnt vmcnt(1)
	v_lshlrev_b32_e32 v60, 16, v64
	v_and_b32_e32 v61, 0xffff0000, v64
	v_lshlrev_b32_e32 v62, 16, v65
	v_and_b32_e32 v63, 0xffff0000, v65
	v_lshlrev_b32_e32 v64, 16, v66
	v_and_b32_e32 v65, 0xffff0000, v66
	v_lshlrev_b32_e32 v66, 16, v67
	v_and_b32_e32 v67, 0xffff0000, v67
	v_pk_add_f32 v[36:37], v[36:37], v[60:61]
	v_pk_add_f32 v[38:39], v[38:39], v[62:63]
	v_pk_add_f32 v[58:59], v[58:59], v[64:65]
	v_pk_add_f32 v[40:41], v[40:41], v[66:67]
	s_waitcnt vmcnt(0)
	v_lshlrev_b32_e32 v72, 16, v68
	v_and_b32_e32 v73, 0xffff0000, v68
	v_lshlrev_b32_e32 v68, 16, v69
	v_and_b32_e32 v69, 0xffff0000, v69
	v_lshlrev_b32_e32 v74, 16, v70
	v_and_b32_e32 v75, 0xffff0000, v70
	v_lshlrev_b32_e32 v70, 16, v71
	v_and_b32_e32 v71, 0xffff0000, v71
	v_pk_add_f32 v[38:39], v[38:39], v[68:69]
	v_pk_add_f32 v[36:37], v[36:37], v[72:73]
	v_pk_add_f32 v[40:41], v[40:41], v[70:71]
	v_pk_add_f32 v[58:59], v[58:59], v[74:75]
